# grid barrier flat release: each XCD leader increments a release word of every XCD after its write-back; all workgroups wait on their own XCD's word (no cross-XCD counter round trip, no leader hand-off
# speedup vs baseline: 1.0136x; 1.0072x over previous
; __device__ __forceinline__ unsigned xb_ld(unsigned* p)              { return __hip_atomic_load(p, __ATOMIC_RELAXED, __HIP_MEMORY_SCOPE_AGENT); }
; __device__ __forceinline__ unsigned xb_add(unsigned* p, unsigned v) { return __hip_atomic_fetch_add(p, v, __ATOMIC_RELAXED, __HIP_MEMORY_SCOPE_AGENT); }
; #define XB_SPIN(cond, bar) do { unsigned _sp = 0; while (cond) { __builtin_amdgcn_s_sleep(1); \
;     if ((++_sp & 255u) == 0u) { if (xb_ld(&(bar)[XB_TMO])) break; if (_sp > XB_SPIN_CAP) { atomicAdd(&(bar)[XB_TMO], 1u); break; } } } } while (0)
; __device__ __forceinline__ void xcd_barrier(const XcdBarrier& b) {
;     ...
;         unsigned nloc = b.st[0], nx = b.st[1];
;         if (nloc == 0u) { xcd_barrier_complete(bar, b.x, nloc, nx); b.st[0] = nloc; b.st[1] = nx; }
;         const unsigned old = xb_add(&bar[XB_XSUB(b.x)], 1u);
;         const unsigned gen = old / nloc;
;         if (old + 1u == (gen + 1u) * nloc) {
;     ...
;             XB_SPIN(xb_ld(&bar[XB_XGEN(b.x)]) == gen, bar);
;             __builtin_amdgcn_fence(__ATOMIC_ACQUIRE, "agent");
;             asm volatile("s_waitcnt vmcnt(0)" ::: "memory");
.LBB0_301:
	s_or_b64 exec, exec, s[6:7]
	v_cvt_f32_u32_e32 v5, v3
	s_waitcnt vmcnt(0)
	buffer_inv sc1
	v_readfirstlane_b32 s5, v4
	v_sub_u32_e32 v4, 0, v3
	v_rcp_iflag_f32_e32 v5, v5
	v_add_u32_e32 v6, s5, v1
	v_mul_f32_e32 v5, 0x4f7ffffe, v5
	v_cvt_u32_f32_e32 v5, v5
	v_mul_lo_u32 v1, v4, v5
	v_mul_hi_u32 v1, v5, v1
	v_add_u32_e32 v1, v5, v1
	v_mul_hi_u32 v1, v6, v1
	v_mul_lo_u32 v4, v1, v3
	v_sub_u32_e32 v4, v6, v4
	v_add_u32_e32 v5, 1, v1
	v_cmp_ge_u32_e32 vcc, v4, v3
	s_nop 1
	v_cndmask_b32_e32 v1, v1, v5, vcc
	v_sub_u32_e32 v5, v4, v3
	v_cndmask_b32_e32 v4, v4, v5, vcc
	v_add_u32_e32 v5, 1, v1
	v_cmp_ge_u32_e32 vcc, v4, v3
	v_add_u32_e32 v4, 1, v6
	s_nop 0
	v_cndmask_b32_e32 v1, v1, v5, vcc
	v_mul_lo_u32 v5, v3, v1
	v_add_u32_e32 v3, v5, v3
	v_cmp_ne_u32_e32 vcc, v4, v3
	s_waitcnt lgkmcnt(0)
	v_add_u32_e32 v16, -1, v1
	v_mul_lo_u32 v16, v16, v2
	s_and_saveexec_b64 s[6:7], vcc
	s_xor_b64 s[6:7], exec, s[6:7]
	s_cbranch_execz .LBB0_315
	v_readlane_b32 s8, v253, 48
	v_readlane_b32 s9, v253, 49
	s_add_u32 s8, s8, 0x3600
	s_addc_u32 s9, s9, 0
	s_waitcnt lgkmcnt(0)
	s_nop 3
	global_load_dword v2, v163, s[8:9] sc1
	s_waitcnt vmcnt(0)
	v_cmp_gt_u32_e32 vcc, v16, v2
	s_and_saveexec_b64 s[8:9], vcc
	s_cbranch_execz .LBB0_314
	s_mov_b32 s5, 1
	s_mov_b64 s[12:13], 0
	s_branch .LBB0_305

; __device__ __forceinline__ unsigned xb_ld(unsigned* p)              { return __hip_atomic_load(p, __ATOMIC_RELAXED, __HIP_MEMORY_SCOPE_AGENT); }
; #define XB_SPIN(cond, bar) do { unsigned _sp = 0; while (cond) { __builtin_amdgcn_s_sleep(1); \
;     if ((++_sp & 255u) == 0u) { if (xb_ld(&(bar)[XB_TMO])) break; if (_sp > XB_SPIN_CAP) { atomicAdd(&(bar)[XB_TMO], 1u); break; } } } } while (0)
; __device__ __forceinline__ void xcd_barrier(const XcdBarrier& b) {
;     ...
;             XB_SPIN(xb_ld(&bar[XB_XGEN(b.x)]) == gen, bar);
.LBB0_309:
	v_readlane_b32 s20, v253, 48
	v_readlane_b32 s21, v253, 49
	s_add_u32 s20, s20, 0x3600
	s_addc_u32 s21, s21, 0
	s_add_i32 s5, s5, 1
	s_mov_b64 s[28:29], -1
	s_nop 2
	global_load_dword v2, v163, s[20:21] sc1
	s_waitcnt vmcnt(0)
	v_cmp_le_u32_e32 vcc, v16, v2
	s_orn2_b64 s[20:21], vcc, exec
	s_branch .LBB0_304

; __device__ __forceinline__ unsigned xb_ld(unsigned* p)              { return __hip_atomic_load(p, __ATOMIC_RELAXED, __HIP_MEMORY_SCOPE_AGENT); }
; __device__ __forceinline__ unsigned xb_add(unsigned* p, unsigned v) { return __hip_atomic_fetch_add(p, v, __ATOMIC_RELAXED, __HIP_MEMORY_SCOPE_AGENT); }
; #define XB_SPIN(cond, bar) do { unsigned _sp = 0; while (cond) { __builtin_amdgcn_s_sleep(1); \
;     if ((++_sp & 255u) == 0u) { if (xb_ld(&(bar)[XB_TMO])) break; if (_sp > XB_SPIN_CAP) { atomicAdd(&(bar)[XB_TMO], 1u); break; } } } } while (0)
; __device__ __forceinline__ void xcd_barrier(const XcdBarrier& b) {
;     ...
;         if (old + 1u == (gen + 1u) * nloc) {
;             __builtin_amdgcn_fence(__ATOMIC_RELEASE, "agent");
;             asm volatile("s_waitcnt vmcnt(0)" ::: "memory");
;             const unsigned og = xb_add(&bar[XB_TOP], 1u);
;             const unsigned tg = og / nx;
;             if (og + 1u == (tg + 1u) * nx) xb_add(&bar[XB_TOPGEN], 1u);
;             else XB_SPIN(xb_ld(&bar[XB_TOPGEN]) == tg, bar);
;             __builtin_amdgcn_fence(__ATOMIC_ACQUIRE, "agent");
;             xb_add(&bar[XB_XGEN(b.x)], 1u);
;             asm volatile("s_waitcnt vmcnt(0)" ::: "memory");
.LBB0_315:
	s_andn2_saveexec_b64 s[6:7], s[6:7]
	s_cbranch_execz .LBB0_335
	s_mov_b64 s[6:7], exec
	buffer_wbl2 sc1
	s_waitcnt lgkmcnt(0)
	s_waitcnt vmcnt(0)
	v_readlane_b32 s18, v253, 48
	v_readlane_b32 s19, v253, 49
	v_readlane_b32 s12, v253, 52
	v_readlane_b32 s13, v253, 53
	s_nop 3
	s_add_u32 s18, s18, 0x3600
	s_addc_u32 s19, s19, 0
	s_add_u32 s12, s12, 0x2500
	s_addc_u32 s13, s13, 0
	global_atomic_add v163, v197, s[12:13]
	global_atomic_add v163, v197, s[12:13] offset:256
	global_atomic_add v163, v197, s[12:13] offset:512
	global_atomic_add v163, v197, s[12:13] offset:768
	global_atomic_add v163, v197, s[12:13] offset:1024
	global_atomic_add v163, v197, s[12:13] offset:1280
	global_atomic_add v163, v197, s[12:13] offset:1536
	global_atomic_add v163, v197, s[12:13] offset:1792
	global_atomic_add v163, v197, s[12:13] offset:2048
	global_atomic_add v163, v197, s[12:13] offset:2304
	global_atomic_add v163, v197, s[12:13] offset:2560
	global_atomic_add v163, v197, s[12:13] offset:2816
	global_atomic_add v163, v197, s[12:13] offset:3072
	global_atomic_add v163, v197, s[12:13] offset:3328
	global_atomic_add v163, v197, s[12:13] offset:3584
	global_atomic_add v163, v197, s[12:13] offset:3840
	s_mov_b32 s5, 0
.Lbar_lead_poll_0:
	global_load_dword v2, v163, s[18:19] sc1
	s_waitcnt vmcnt(0)
	v_cmp_le_u32_e32 vcc, v16, v2
	s_cbranch_vccnz .Lbar_lead_done_0
	s_sleep 1
	s_add_i32 s5, s5, 1
	s_cmp_lt_u32 s5, 0x40000
	s_cbranch_scc1 .Lbar_lead_poll_0
.Lbar_lead_done_0:
.LBB0_335:
	s_or_b64 exec, exec, s[0:1]
	s_waitcnt lgkmcnt(0)
	s_barrier

; __device__ __forceinline__ unsigned xb_ld(unsigned* p)              { return __hip_atomic_load(p, __ATOMIC_RELAXED, __HIP_MEMORY_SCOPE_AGENT); }
; __device__ __forceinline__ unsigned xb_add(unsigned* p, unsigned v) { return __hip_atomic_fetch_add(p, v, __ATOMIC_RELAXED, __HIP_MEMORY_SCOPE_AGENT); }
; #define XB_SPIN(cond, bar) do { unsigned _sp = 0; while (cond) { __builtin_amdgcn_s_sleep(1); \
;     if ((++_sp & 255u) == 0u) { if (xb_ld(&(bar)[XB_TMO])) break; if (_sp > XB_SPIN_CAP) { atomicAdd(&(bar)[XB_TMO], 1u); break; } } } } while (0)
; __device__ __forceinline__ void xcd_barrier(const XcdBarrier& b) {
;     ...
;         unsigned nloc = b.st[0], nx = b.st[1];
;         if (nloc == 0u) { xcd_barrier_complete(bar, b.x, nloc, nx); b.st[0] = nloc; b.st[1] = nx; }
;         const unsigned old = xb_add(&bar[XB_XSUB(b.x)], 1u);
;         const unsigned gen = old / nloc;
;         if (old + 1u == (gen + 1u) * nloc) {
;     ...
;             XB_SPIN(xb_ld(&bar[XB_XGEN(b.x)]) == gen, bar);
;             __builtin_amdgcn_fence(__ATOMIC_ACQUIRE, "agent");
;             asm volatile("s_waitcnt vmcnt(0)" ::: "memory");
.LBB0_1538:
	s_or_b64 exec, exec, s[6:7]
	v_cvt_f32_u32_e32 v5, v3
	s_waitcnt vmcnt(0)
	buffer_inv sc1
	v_readfirstlane_b32 s4, v4
	v_sub_u32_e32 v4, 0, v3
	v_rcp_iflag_f32_e32 v5, v5
	v_add_u32_e32 v6, s4, v1
	v_mul_f32_e32 v5, 0x4f7ffffe, v5
	v_cvt_u32_f32_e32 v5, v5
	v_mul_lo_u32 v1, v4, v5
	v_mul_hi_u32 v1, v5, v1
	v_add_u32_e32 v1, v5, v1
	v_mul_hi_u32 v1, v6, v1
	v_mul_lo_u32 v4, v1, v3
	v_sub_u32_e32 v4, v6, v4
	v_add_u32_e32 v5, 1, v1
	v_cmp_ge_u32_e32 vcc, v4, v3
	s_nop 1
	v_cndmask_b32_e32 v1, v1, v5, vcc
	v_sub_u32_e32 v5, v4, v3
	v_cndmask_b32_e32 v4, v4, v5, vcc
	v_add_u32_e32 v5, 1, v1
	v_cmp_ge_u32_e32 vcc, v4, v3
	v_add_u32_e32 v4, 1, v6
	s_nop 0
	v_cndmask_b32_e32 v1, v1, v5, vcc
	v_mul_lo_u32 v5, v3, v1
	v_add_u32_e32 v3, v5, v3
	v_cmp_ne_u32_e32 vcc, v4, v3
	s_waitcnt lgkmcnt(0)
	v_add_u32_e32 v16, -1, v1
	v_mul_lo_u32 v16, v16, v2
	s_and_saveexec_b64 s[4:5], vcc
	s_xor_b64 s[6:7], exec, s[4:5]
	s_cbranch_execz .LBB0_1552
	v_readlane_b32 s4, v253, 48
	v_readlane_b32 s5, v253, 49
	s_add_u32 s4, s4, 0x3600
	s_addc_u32 s5, s5, 0
	s_waitcnt lgkmcnt(0)
	s_nop 3
	global_load_dword v2, v163, s[4:5] sc1
	s_waitcnt vmcnt(0)
	v_cmp_gt_u32_e32 vcc, v16, v2
	s_and_saveexec_b64 s[8:9], vcc
	s_cbranch_execz .LBB0_1551
	s_mov_b32 s4, 1
	s_mov_b64 s[12:13], 0
	s_branch .LBB0_1542

; __device__ __forceinline__ unsigned xb_ld(unsigned* p)              { return __hip_atomic_load(p, __ATOMIC_RELAXED, __HIP_MEMORY_SCOPE_AGENT); }
; #define XB_SPIN(cond, bar) do { unsigned _sp = 0; while (cond) { __builtin_amdgcn_s_sleep(1); \
;     if ((++_sp & 255u) == 0u) { if (xb_ld(&(bar)[XB_TMO])) break; if (_sp > XB_SPIN_CAP) { atomicAdd(&(bar)[XB_TMO], 1u); break; } } } } while (0)
; __device__ __forceinline__ void xcd_barrier(const XcdBarrier& b) {
;     ...
;             XB_SPIN(xb_ld(&bar[XB_XGEN(b.x)]) == gen, bar);
.LBB0_1546:
	v_readlane_b32 s20, v253, 48
	v_readlane_b32 s21, v253, 49
	s_add_u32 s20, s20, 0x3600
	s_addc_u32 s21, s21, 0
	s_add_i32 s4, s4, 1
	s_mov_b64 s[28:29], -1
	s_nop 2
	global_load_dword v2, v163, s[20:21] sc1
	s_waitcnt vmcnt(0)
	v_cmp_le_u32_e32 vcc, v16, v2
	s_orn2_b64 s[20:21], vcc, exec
	s_branch .LBB0_1541

; __device__ __forceinline__ unsigned xb_ld(unsigned* p)              { return __hip_atomic_load(p, __ATOMIC_RELAXED, __HIP_MEMORY_SCOPE_AGENT); }
; __device__ __forceinline__ unsigned xb_add(unsigned* p, unsigned v) { return __hip_atomic_fetch_add(p, v, __ATOMIC_RELAXED, __HIP_MEMORY_SCOPE_AGENT); }
; #define XB_SPIN(cond, bar) do { unsigned _sp = 0; while (cond) { __builtin_amdgcn_s_sleep(1); \
;     if ((++_sp & 255u) == 0u) { if (xb_ld(&(bar)[XB_TMO])) break; if (_sp > XB_SPIN_CAP) { atomicAdd(&(bar)[XB_TMO], 1u); break; } } } } while (0)
; __device__ __forceinline__ void xcd_barrier(const XcdBarrier& b) {
;     ...
;         if (old + 1u == (gen + 1u) * nloc) {
;             __builtin_amdgcn_fence(__ATOMIC_RELEASE, "agent");
;             asm volatile("s_waitcnt vmcnt(0)" ::: "memory");
;             const unsigned og = xb_add(&bar[XB_TOP], 1u);
;             const unsigned tg = og / nx;
;             if (og + 1u == (tg + 1u) * nx) xb_add(&bar[XB_TOPGEN], 1u);
;             else XB_SPIN(xb_ld(&bar[XB_TOPGEN]) == tg, bar);
;             __builtin_amdgcn_fence(__ATOMIC_ACQUIRE, "agent");
;             xb_add(&bar[XB_XGEN(b.x)], 1u);
.LBB0_1553:
	s_mov_b64 s[6:7], exec
	buffer_wbl2 sc1
	s_waitcnt lgkmcnt(0)
	s_waitcnt vmcnt(0)
	v_readlane_b32 s18, v253, 48
	v_readlane_b32 s19, v253, 49
	v_readlane_b32 s12, v253, 52
	v_readlane_b32 s13, v253, 53
	s_nop 3
	s_add_u32 s18, s18, 0x3600
	s_addc_u32 s19, s19, 0
	s_add_u32 s12, s12, 0x2500
	s_addc_u32 s13, s13, 0
	global_atomic_add v163, v197, s[12:13]
	global_atomic_add v163, v197, s[12:13] offset:256
	global_atomic_add v163, v197, s[12:13] offset:512
	global_atomic_add v163, v197, s[12:13] offset:768
	global_atomic_add v163, v197, s[12:13] offset:1024
	global_atomic_add v163, v197, s[12:13] offset:1280
	global_atomic_add v163, v197, s[12:13] offset:1536
	global_atomic_add v163, v197, s[12:13] offset:1792
	global_atomic_add v163, v197, s[12:13] offset:2048
	global_atomic_add v163, v197, s[12:13] offset:2304
	global_atomic_add v163, v197, s[12:13] offset:2560
	global_atomic_add v163, v197, s[12:13] offset:2816
	global_atomic_add v163, v197, s[12:13] offset:3072
	global_atomic_add v163, v197, s[12:13] offset:3328
	global_atomic_add v163, v197, s[12:13] offset:3584
	global_atomic_add v163, v197, s[12:13] offset:3840
	s_mov_b32 s5, 0

; __device__ __forceinline__ unsigned xb_ld(unsigned* p)              { return __hip_atomic_load(p, __ATOMIC_RELAXED, __HIP_MEMORY_SCOPE_AGENT); }
; __device__ __forceinline__ unsigned xb_add(unsigned* p, unsigned v) { return __hip_atomic_fetch_add(p, v, __ATOMIC_RELAXED, __HIP_MEMORY_SCOPE_AGENT); }
; #define XB_SPIN(cond, bar) do { unsigned _sp = 0; while (cond) { __builtin_amdgcn_s_sleep(1); \
;     if ((++_sp & 255u) == 0u) { if (xb_ld(&(bar)[XB_TMO])) break; if (_sp > XB_SPIN_CAP) { atomicAdd(&(bar)[XB_TMO], 1u); break; } } } } while (0)
; __device__ __forceinline__ void xcd_barrier(const XcdBarrier& b) {
;     ...
;             else XB_SPIN(xb_ld(&bar[XB_TOPGEN]) == tg, bar);
;             __builtin_amdgcn_fence(__ATOMIC_ACQUIRE, "agent");
;             xb_add(&bar[XB_XGEN(b.x)], 1u);
;             asm volatile("s_waitcnt vmcnt(0)" ::: "memory");
.Lbar_lead_done_12:
	s_mov_b64 s[8:9], 0
	s_getpc_b64 s[98:99]
